# v42 + RMS-norm lane butterflies: lower four hops by DPP adds instead of LDS bpermute
# speedup vs baseline: 1.0082x; 1.0082x over previous
; __device__ __forceinline__ float wave_sum(float v) {
; #pragma unroll
;     for (int o = 1; o < 64; o <<= 1) v += __shfl_xor(v, o);
;     return v;
; __device__ __forceinline__ void norm_mod_row_f8(const float* xrow, const float* A, const float* B, unsigned char* orow, int lane) {
;     ...
; #pragma unroll
;     for (int j = 0; j < 4; ++j) { v[2 * j] = *(const f32x4*)((const char*)(xrow + 512 * j) + l32); v[2 * j + 1] = *(const f32x4*)((const char*)(xrow + 512 * j + 4) + l32); }
; #pragma unroll
;     for (int j = 0; j < 8; ++j) s += (v[j].x * v[j].x + v[j].y * v[j].y) + (v[j].z * v[j].z + v[j].w * v[j].w);
;     const float rstd = 1.f / sqrtf(wave_sum(s) * (1.f / DM) + EPS_);
.LBB0_201:
	global_load_dwordx4 v[30:33], v[52:53], off offset:-4096
	global_load_dwordx4 v[26:29], v[52:53], off offset:-4080
	global_load_dwordx4 v[18:21], v[52:53], off offset:-2048
	global_load_dwordx4 v[14:17], v[52:53], off
	global_load_dwordx4 v[22:25], v[52:53], off offset:-2032
	global_load_dwordx4 v[10:13], v[52:53], off offset:16
	global_load_dwordx4 v[2:5], v[52:53], off offset:2064
	global_load_dwordx4 v[6:9], v[52:53], off offset:2048
	global_load_dwordx4 v[62:65], v[34:35], off offset:16
	global_load_dwordx4 v[66:69], v[34:35], off
	global_load_dwordx4 v[70:73], v[36:37], off offset:16
	global_load_dwordx4 v[74:77], v[36:37], off
	v_mov_b32_e32 v78, 0
	v_mov_b32_e32 v79, 0
	s_add_i32 s8, s8, s26
	v_lshl_add_u64 v[52:53], v[52:53], 0, s[12:13]
	s_cmpk_lt_i32 s8, 0x4000
	s_waitcnt vmcnt(11)
	v_mov_b32_e32 v82, v31
	s_waitcnt vmcnt(10)
	v_mov_b32_e32 v83, v27
	v_mov_b32_e32 v86, v33
	v_mov_b32_e32 v87, v29
	v_mov_b32_e32 v80, v30
	v_mov_b32_e32 v81, v26
	v_mov_b32_e32 v84, v32
	v_mov_b32_e32 v85, v28
	s_waitcnt vmcnt(9)
	v_pk_mul_f32 v[88:89], v[20:21], v[20:21]
	v_pk_mul_f32 v[90:91], v[18:19], v[18:19]
	v_pk_mul_f32 v[82:83], v[82:83], v[82:83]
	v_pk_mul_f32 v[86:87], v[86:87], v[86:87]
	v_pk_mov_b32 v[104:105], v[90:91], v[88:89] op_sel:[1,0]
	v_mov_b32_e32 v91, v89
	v_pk_fma_f32 v[80:81], v[80:81], v[80:81], v[82:83]
	v_pk_fma_f32 v[82:83], v[84:85], v[84:85], v[86:87]
	s_waitcnt vmcnt(7)
	v_mul_f32_e32 v92, v23, v23
	v_mul_f32_e32 v94, v25, v25
	v_pk_add_f32 v[84:85], v[104:105], v[90:91]
	v_pk_add_f32 v[80:81], v[80:81], v[82:83]
	v_mul_f32_e32 v103, v14, v14
	v_mul_f32_e32 v106, v15, v15
	v_mul_f32_e32 v107, v16, v16
	v_mul_f32_e32 v108, v17, v17
	v_pk_fma_f32 v[88:89], v[22:23], v[22:23], v[92:93] op_sel_hi:[1,1,0]
	v_pk_fma_f32 v[92:93], v[24:25], v[24:25], v[94:95] op_sel_hi:[1,1,0]
	v_pk_add_f32 v[82:83], v[84:85], v[84:85] op_sel:[0,1] op_sel_hi:[1,0]
	v_pk_add_f32 v[80:81], v[80:81], v[80:81] op_sel:[0,1] op_sel_hi:[1,0]
	s_waitcnt vmcnt(6)
	v_pk_mul_f32 v[96:97], v[12:13], v[12:13]
	v_pk_mul_f32 v[98:99], v[10:11], v[10:11]
	v_mov_b32_e32 v89, v107
	v_mov_b32_e32 v93, v108
	v_mov_b32_e32 v83, v106
	v_mov_b32_e32 v81, v103
	v_pk_mov_b32 v[94:95], v[98:99], v[96:97] op_sel:[1,0]
	v_mov_b32_e32 v99, v97
	v_pk_add_f32 v[84:85], v[88:89], v[92:93]
	v_pk_add_f32 v[80:81], v[80:81], v[82:83]
	s_waitcnt vmcnt(4)
	v_mul_f32_e32 v100, v7, v7
	v_mul_f32_e32 v102, v9, v9
	v_pk_add_f32 v[86:87], v[94:95], v[98:99]
	v_pk_add_f32 v[80:81], v[80:81], v[84:85]
	v_mul_f32_e32 v109, v2, v2
	v_mul_f32_e32 v110, v3, v3
	v_mul_f32_e32 v111, v4, v4
	v_mul_f32_e32 v112, v5, v5
	v_pk_fma_f32 v[96:97], v[6:7], v[6:7], v[100:101] op_sel_hi:[1,1,0]
	v_pk_fma_f32 v[100:101], v[8:9], v[8:9], v[102:103] op_sel_hi:[1,1,0]
	v_pk_add_f32 v[86:87], v[86:87], v[86:87] op_sel:[0,1] op_sel_hi:[1,0]
	v_pk_add_f32 v[80:81], v[80:81], v[80:81] op_sel:[0,1] op_sel_hi:[1,0]
	v_mov_b32_e32 v97, v111
	v_mov_b32_e32 v101, v112
	v_mov_b32_e32 v87, v110
	v_mov_b32_e32 v81, v109
	v_pk_add_f32 v[88:89], v[96:97], v[100:101]
	v_pk_add_f32 v[80:81], v[80:81], v[86:87]
	s_nop 0
	v_pk_add_f32 v[80:81], v[80:81], v[88:89]
	s_nop 0
	v_add_f32_e32 v80, v80, v81
	s_waitcnt lgkmcnt(0)
	s_nop 1
	v_add_f32_dpp v80, v80, v80 quad_perm:[1,0,3,2] row_mask:0xf bank_mask:0xf bound_ctrl:1
	s_waitcnt lgkmcnt(0)
	s_nop 1
	v_add_f32_dpp v80, v80, v80 quad_perm:[2,3,0,1] row_mask:0xf bank_mask:0xf bound_ctrl:1
	s_waitcnt lgkmcnt(0)
	s_nop 1
	v_add_f32_dpp v80, v80, v80 row_half_mirror row_mask:0xf bank_mask:0xf bound_ctrl:1
	s_waitcnt lgkmcnt(0)
	s_nop 1
	v_add_f32_dpp v80, v80, v80 row_mirror row_mask:0xf bank_mask:0xf bound_ctrl:1
	ds_bpermute_b32 v81, v57, v80
	s_waitcnt lgkmcnt(0)
	v_add_f32_e32 v80, v80, v81
	ds_bpermute_b32 v81, v58, v80
	s_waitcnt lgkmcnt(0)
	v_add_f32_e32 v80, v80, v81
	v_fmamk_f32 v80, v80, 0x3a000000, v59
	v_mul_f32_e32 v81, 0x4f800000, v80
	v_cmp_gt_f32_e32 vcc, s9, v80
	s_nop 1
	v_cndmask_b32_e32 v80, v80, v81, vcc
	v_sqrt_f32_e32 v81, v80
	s_nop 0
	v_add_u32_e32 v82, -1, v81
	v_add_u32_e32 v83, 1, v81
	v_fma_f32 v84, -v82, v81, v80
	v_fma_f32 v85, -v83, v81, v80
	v_cmp_ge_f32_e64 s[4:5], 0, v84
	s_nop 1
	v_cndmask_b32_e64 v81, v81, v82, s[4:5]
	v_cmp_lt_f32_e64 s[4:5], 0, v85
	s_nop 1
	v_cndmask_b32_e64 v81, v81, v83, s[4:5]
	v_mul_f32_e32 v82, 0x37800000, v81
	v_cndmask_b32_e32 v81, v81, v82, vcc
	v_cmp_class_f32_e32 vcc, v80, v60
	s_nop 1
	v_cndmask_b32_e32 v80, v81, v80, vcc
	v_div_scale_f32 v81, s[4:5], v80, v80, 1.0
	v_rcp_f32_e32 v83, v81
	v_div_scale_f32 v82, vcc, 1.0, v80, 1.0
	v_fma_f32 v84, -v81, v83, 1.0
	v_fmac_f32_e32 v83, v84, v83
	v_mul_f32_e32 v84, v82, v83
	v_fma_f32 v85, -v81, v84, v82
	v_fmac_f32_e32 v84, v85, v83
	v_fma_f32 v81, -v81, v84, v82
	v_div_fmas_f32 v81, v81, v83, v84
	v_div_fixup_f32 v80, v81, v80, 1.0
	v_pk_mul_f32 v[30:31], v[30:31], v[80:81] op_sel_hi:[1,0]
	v_pk_mul_f32 v[26:27], v[26:27], v[80:81] op_sel_hi:[1,0]
	s_waitcnt vmcnt(0)
; __device__ __forceinline__ void norm_mod_row_f8(const float* xrow, const float* A, const float* B, unsigned char* orow, int lane) {
;     ...
;     for (int j = 0; j < 4; ++j) {
;         const f32x4 a0 = *(const f32x4*)((const char*)(A + 512 * j) + l32), a1 = *(const f32x4*)((const char*)(A + 512 * j + 4) + l32);
;         const f32x4 b0 = *(const f32x4*)((const char*)(B + 512 * j) + l32), b1 = *(const f32x4*)((const char*)(B + 512 * j + 4) + l32);
;         u32x2 q8; q8.x = pg8::pack4_fp8(v[2 * j] * rstd * a0 + b0, pg8::F8_SH); q8.y = pg8::pack4_fp8(v[2 * j + 1] * rstd * a1 + b1, pg8::F8_SH);
;         *(u32x2*)((char*)(orow + 512 * j) + l8) = q8; }
	v_pk_fma_f32 v[30:31], v[66:67], v[30:31], v[74:75]
	v_pk_fma_f32 v[26:27], v[62:63], v[26:27], v[70:71]
	v_med3_f32 v30, v30, s14, v61
	v_med3_f32 v31, v31, s14, v61
	v_med3_f32 v26, v26, s14, v61
	v_med3_f32 v27, v27, s14, v61
	v_cvt_pk_fp8_f32 v78, v30, v31
	v_cvt_pk_fp8_f32 v79, v26, v27
	v_pk_mul_f32 v[32:33], v[32:33], v[80:81] op_sel_hi:[1,0]
	v_pk_mul_f32 v[28:29], v[28:29], v[80:81] op_sel_hi:[1,0]
	v_pk_fma_f32 v[32:33], v[68:69], v[32:33], v[76:77]
	v_pk_fma_f32 v[28:29], v[64:65], v[28:29], v[72:73]
	v_med3_f32 v32, v32, s14, v61
	v_med3_f32 v33, v33, s14, v61
	v_med3_f32 v28, v28, s14, v61
	v_med3_f32 v29, v29, s14, v61
	v_cvt_pk_fp8_f32 v78, v32, v33 op_sel:[0,0,1]
	v_cvt_pk_fp8_f32 v79, v28, v29 op_sel:[0,0,1]
	v_pk_mul_f32 v[18:19], v[18:19], v[80:81] op_sel_hi:[1,0]
	v_pk_mul_f32 v[22:23], v[22:23], v[80:81] op_sel_hi:[1,0]
	v_mov_b32_e32 v70, 0
	global_store_dwordx2 v[50:51], v[78:79], off
	global_load_dwordx4 v[26:29], v[40:41], off
	global_load_dwordx4 v[30:33], v[38:39], off
	global_load_dwordx4 v[62:65], v[38:39], off offset:16
	global_load_dwordx4 v[66:69], v[40:41], off offset:16
	v_mov_b32_e32 v71, 0
	v_pk_mul_f32 v[20:21], v[20:21], v[80:81] op_sel_hi:[1,0]
	v_pk_mul_f32 v[24:25], v[24:25], v[80:81] op_sel_hi:[1,0]
	v_pk_mul_f32 v[14:15], v[14:15], v[80:81] op_sel_hi:[1,0]
	v_pk_mul_f32 v[10:11], v[10:11], v[80:81] op_sel_hi:[1,0]
	v_pk_mul_f32 v[16:17], v[16:17], v[80:81] op_sel_hi:[1,0]
	v_pk_mul_f32 v[12:13], v[12:13], v[80:81] op_sel_hi:[1,0]
	v_pk_mul_f32 v[6:7], v[6:7], v[80:81] op_sel_hi:[1,0]
	v_pk_mul_f32 v[2:3], v[2:3], v[80:81] op_sel_hi:[1,0]
	v_pk_mul_f32 v[8:9], v[8:9], v[80:81] op_sel_hi:[1,0]
	v_pk_mul_f32 v[4:5], v[4:5], v[80:81] op_sel_hi:[1,0]
	s_waitcnt vmcnt(2)
	v_pk_fma_f32 v[18:19], v[18:19], v[30:31], v[26:27]
	s_nop 0
	v_med3_f32 v18, v18, s14, v61
	s_waitcnt vmcnt(0)
	v_pk_fma_f32 v[22:23], v[22:23], v[62:63], v[66:67]
	v_med3_f32 v19, v19, s14, v61
	v_med3_f32 v22, v22, s14, v61
	v_med3_f32 v23, v23, s14, v61
	v_cvt_pk_fp8_f32 v70, v18, v19
	v_cvt_pk_fp8_f32 v71, v22, v23
	v_pk_fma_f32 v[20:21], v[20:21], v[32:33], v[28:29]
	v_pk_fma_f32 v[24:25], v[24:25], v[64:65], v[68:69]
	v_med3_f32 v20, v20, s14, v61
	v_med3_f32 v21, v21, s14, v61
	v_med3_f32 v24, v24, s14, v61
	v_med3_f32 v25, v25, s14, v61
	v_cvt_pk_fp8_f32 v70, v20, v21 op_sel:[0,0,1]
	v_cvt_pk_fp8_f32 v71, v24, v25 op_sel:[0,0,1]
	v_mov_b32_e32 v62, 0
	v_mov_b32_e32 v63, 0
	global_store_dwordx2 v[50:51], v[70:71], off offset:512
	global_load_dwordx4 v[18:21], v[44:45], off
	global_load_dwordx4 v[22:25], v[42:43], off
	global_load_dwordx4 v[26:29], v[42:43], off offset:16
	global_load_dwordx4 v[30:33], v[44:45], off offset:16
	s_waitcnt vmcnt(2)
	v_pk_fma_f32 v[14:15], v[14:15], v[22:23], v[18:19]
	s_nop 0
	v_med3_f32 v14, v14, s14, v61
	s_waitcnt vmcnt(0)
	v_pk_fma_f32 v[10:11], v[10:11], v[26:27], v[30:31]
	v_med3_f32 v15, v15, s14, v61
	v_med3_f32 v10, v10, s14, v61
	v_med3_f32 v11, v11, s14, v61
	v_cvt_pk_fp8_f32 v62, v14, v15
	v_cvt_pk_fp8_f32 v63, v10, v11
	v_pk_fma_f32 v[16:17], v[16:17], v[24:25], v[20:21]
	v_pk_fma_f32 v[12:13], v[12:13], v[28:29], v[32:33]
	v_med3_f32 v16, v16, s14, v61
	v_med3_f32 v17, v17, s14, v61
	v_med3_f32 v12, v12, s14, v61
	v_med3_f32 v13, v13, s14, v61
	v_cvt_pk_fp8_f32 v62, v16, v17 op_sel:[0,0,1]
	v_cvt_pk_fp8_f32 v63, v12, v13 op_sel:[0,0,1]
	v_mov_b32_e32 v26, 0
	v_mov_b32_e32 v27, 0
	global_store_dwordx2 v[50:51], v[62:63], off offset:1024
	global_load_dwordx4 v[10:13], v[48:49], off
	global_load_dwordx4 v[14:17], v[46:47], off
	global_load_dwordx4 v[18:21], v[46:47], off offset:16
	global_load_dwordx4 v[22:25], v[48:49], off offset:16
	s_waitcnt vmcnt(2)
	v_pk_fma_f32 v[6:7], v[6:7], v[14:15], v[10:11]
	s_nop 0
	v_med3_f32 v6, v6, s14, v61
	s_waitcnt vmcnt(0)
	v_pk_fma_f32 v[2:3], v[2:3], v[18:19], v[22:23]
	v_med3_f32 v7, v7, s14, v61
	v_med3_f32 v2, v2, s14, v61
	v_med3_f32 v3, v3, s14, v61
	v_cvt_pk_fp8_f32 v26, v6, v7
	v_cvt_pk_fp8_f32 v27, v2, v3
	v_pk_fma_f32 v[8:9], v[8:9], v[16:17], v[12:13]
	v_pk_fma_f32 v[4:5], v[4:5], v[20:21], v[24:25]
	v_med3_f32 v8, v8, s14, v61
	v_med3_f32 v9, v9, s14, v61
	v_med3_f32 v4, v4, s14, v61
	v_med3_f32 v2, v5, s14, v61
	v_cvt_pk_fp8_f32 v26, v8, v9 op_sel:[0,0,1]
	v_cvt_pk_fp8_f32 v27, v4, v2 op_sel:[0,0,1]
	global_store_dwordx2 v[50:51], v[26:27], off offset:1536
	v_lshl_add_u64 v[50:51], v[50:51], 0, s[10:11]
	s_cbranch_scc1 .LBB0_201

; __device__ __forceinline__ float wave_sum(float v) {
; #pragma unroll
;     for (int o = 1; o < 64; o <<= 1) v += __shfl_xor(v, o);
;     return v;
; __device__ __forceinline__ void p3_prep(Frame& F) {
;     ...
;         { const u32x4 w = *(const u32x4*)(pr + 3072 + 8 * lane); float s = 0.f;
; #pragma unroll
;           for (int i = 0; i < 4; ++i) { const float a = bf_lo(w[i]), b = bf_hi(w[i]); s += a * a + b * b; }
;           s = wave_sum(s); if (lane == 0) WSP(float, WS_RQ)[t] = 1.f / sqrtf(s * (1.f / 512.f) + EPS_); }
.LBB0_341:
	s_waitcnt lgkmcnt(0)
	v_lshl_add_u64 v[12:13], s[22:23], 0, v[8:9]
	v_add_co_u32_e32 v30, vcc, 0x1f701000, v12
	s_nop 1
	v_addc_co_u32_e32 v31, vcc, 0, v13, vcc
	global_load_dwordx4 v[30:33], v[30:31], off offset:2048
	s_waitcnt vmcnt(0)
	v_lshlrev_b32_e32 v4, 16, v30
	v_and_b32_e32 v29, 0xffff0000, v30
	v_lshlrev_b32_e32 v30, 16, v31
	v_and_b32_e32 v31, 0xffff0000, v31
	v_lshlrev_b32_e32 v34, 16, v32
	v_and_b32_e32 v32, 0xffff0000, v32
	v_mul_f32_e32 v29, v29, v29
	v_mul_f32_e32 v31, v31, v31
	v_lshlrev_b32_e32 v35, 16, v33
	v_and_b32_e32 v33, 0xffff0000, v33
	v_mul_f32_e32 v32, v32, v32
	v_fmac_f32_e32 v29, v4, v4
	v_fmac_f32_e32 v31, v30, v30
	v_mul_f32_e32 v33, v33, v33
	v_fmac_f32_e32 v32, v34, v34
	v_add_f32_e32 v4, v29, v31
	v_add_f32_e32 v4, v32, v4
	v_fmac_f32_e32 v33, v35, v35
	v_add_f32_e32 v4, v33, v4
	s_waitcnt lgkmcnt(0)
	s_nop 1
	v_add_f32_dpp v4, v4, v4 quad_perm:[1,0,3,2] row_mask:0xf bank_mask:0xf bound_ctrl:1
	s_waitcnt lgkmcnt(0)
	s_nop 1
	v_add_f32_dpp v4, v4, v4 quad_perm:[2,3,0,1] row_mask:0xf bank_mask:0xf bound_ctrl:1
	s_waitcnt lgkmcnt(0)
	s_nop 1
	v_add_f32_dpp v4, v4, v4 row_half_mirror row_mask:0xf bank_mask:0xf bound_ctrl:1
	s_waitcnt lgkmcnt(0)
	s_nop 1
	v_add_f32_dpp v4, v4, v4 row_mirror row_mask:0xf bank_mask:0xf bound_ctrl:1
	ds_bpermute_b32 v29, v17, v4
	s_waitcnt lgkmcnt(0)
	v_add_f32_e32 v4, v4, v29
	ds_bpermute_b32 v29, v18, v4
	s_and_saveexec_b64 s[10:11], s[4:5]
	s_cbranch_execz .LBB0_343
	s_waitcnt lgkmcnt(0)
	v_add_f32_e32 v4, v4, v29
	v_fmamk_f32 v4, v4, 0x3b000000, v20
	v_mul_f32_e32 v29, 0x4f800000, v4
	v_cmp_gt_f32_e32 vcc, s19, v4
	s_nop 1
	v_cndmask_b32_e32 v4, v4, v29, vcc
	v_sqrt_f32_e32 v29, v4
	s_nop 0
	v_add_u32_e32 v30, -1, v29
	v_fma_f32 v32, -v30, v29, v4
	v_add_u32_e32 v31, 1, v29
	v_cmp_ge_f32_e64 s[8:9], 0, v32
	s_nop 1
	v_cndmask_b32_e64 v30, v29, v30, s[8:9]
	v_fma_f32 v29, -v31, v29, v4
	v_cmp_lt_f32_e64 s[8:9], 0, v29
	s_nop 1
	v_cndmask_b32_e64 v29, v30, v31, s[8:9]
	v_mul_f32_e32 v30, 0x37800000, v29
	v_cndmask_b32_e32 v29, v29, v30, vcc
	v_cmp_class_f32_e32 vcc, v4, v21
	s_nop 1
	v_cndmask_b32_e32 v4, v29, v4, vcc
	v_div_scale_f32 v29, s[8:9], v4, v4, 1.0
	v_rcp_f32_e32 v30, v29
	s_add_u32 s8, s22, s24
	s_addc_u32 s9, s23, s25
	v_fma_f32 v31, -v29, v30, 1.0
	v_fmac_f32_e32 v30, v31, v30
	v_div_scale_f32 v31, vcc, 1.0, v4, 1.0
	v_mul_f32_e32 v32, v31, v30
	v_fma_f32 v33, -v29, v32, v31
	v_fmac_f32_e32 v32, v33, v30
	v_fma_f32 v29, -v29, v32, v31
	v_div_fmas_f32 v29, v29, v30, v32
	v_div_fixup_f32 v4, v29, v4, 1.0
	global_store_dword v22, v4, s[8:9]

; __device__ __forceinline__ void p3_prep(Frame& F) {
;     ...
;         { float s = 0.f; if (lane < 32) { const u32x4 w = *(const u32x4*)(pr + 3584 + 8 * lane);
; #pragma unroll
;               for (int i = 0; i < 4; ++i) { const float a = bf_lo(w[i]), b = bf_hi(w[i]); s += a * a + b * b; } }
;           s = wave_sum(s); if (lane == 0) WSP(float, WS_RKV)[t] = 1.f / sqrtf(s * (1.f / 256.f) + EPS_); }
.LBB0_345:
	s_or_b64 exec, exec, s[8:9]
	s_waitcnt lgkmcnt(0)
	s_nop 1
	v_add_f32_dpp v4, v4, v4 quad_perm:[1,0,3,2] row_mask:0xf bank_mask:0xf bound_ctrl:1
	s_waitcnt lgkmcnt(0)
	s_nop 1
	v_add_f32_dpp v4, v4, v4 quad_perm:[2,3,0,1] row_mask:0xf bank_mask:0xf bound_ctrl:1
	s_waitcnt lgkmcnt(0)
	s_nop 1
	v_add_f32_dpp v4, v4, v4 row_half_mirror row_mask:0xf bank_mask:0xf bound_ctrl:1
	s_waitcnt lgkmcnt(0)
	s_nop 1
	v_add_f32_dpp v4, v4, v4 row_mirror row_mask:0xf bank_mask:0xf bound_ctrl:1
	ds_bpermute_b32 v12, v17, v4
	s_waitcnt lgkmcnt(0)
	v_add_f32_e32 v4, v4, v12
	ds_bpermute_b32 v12, v18, v4
	s_and_saveexec_b64 s[10:11], s[4:5]
	s_cbranch_execz .LBB0_347
	s_waitcnt lgkmcnt(0)
	v_add_f32_e32 v4, v4, v12
	v_fmamk_f32 v4, v4, 0x3b800000, v20
	v_mul_f32_e32 v12, 0x4f800000, v4
	v_cmp_gt_f32_e32 vcc, s19, v4
	s_nop 1
	v_cndmask_b32_e32 v4, v4, v12, vcc
	v_sqrt_f32_e32 v12, v4
	s_nop 0
	v_add_u32_e32 v13, -1, v12
	v_fma_f32 v30, -v13, v12, v4
	v_add_u32_e32 v29, 1, v12
	v_cmp_ge_f32_e64 s[8:9], 0, v30
	s_nop 1
	v_cndmask_b32_e64 v13, v12, v13, s[8:9]
	v_fma_f32 v12, -v29, v12, v4
	v_cmp_lt_f32_e64 s[8:9], 0, v12
	s_nop 1
	v_cndmask_b32_e64 v12, v13, v29, s[8:9]
	v_mul_f32_e32 v13, 0x37800000, v12
	v_cndmask_b32_e32 v12, v12, v13, vcc
	v_cmp_class_f32_e32 vcc, v4, v21
	s_nop 1
	v_cndmask_b32_e32 v4, v12, v4, vcc
	v_div_scale_f32 v12, s[8:9], v4, v4, 1.0
	v_rcp_f32_e32 v13, v12
	s_add_u32 s8, s22, s24
	s_addc_u32 s9, s23, s25
	v_fma_f32 v29, -v12, v13, 1.0
	v_fmac_f32_e32 v13, v29, v13
	v_div_scale_f32 v29, vcc, 1.0, v4, 1.0
	v_mul_f32_e32 v30, v29, v13
	v_fma_f32 v31, -v12, v30, v29
	v_fmac_f32_e32 v30, v31, v13
	v_fma_f32 v12, -v12, v30, v29
	v_div_fmas_f32 v12, v12, v13, v30
	v_div_fixup_f32 v4, v12, v4, 1.0
	global_store_dword v23, v4, s[8:9]

; __device__ __forceinline__ void p6_mix(Frame& F) {
;     ...
;     for (int t = gw; t < S_; t += NGW) {
;         const int h = lane >> 3; float ls[3], mx = -1e30f;
; #pragma unroll
;         for (int p = 0; p < 3; ++p) { ls[p] = WSP(float, WS_LSE)[((size_t)p * S_ + t) * 8 + h]; mx = fmaxf(mx, ls[p]); }
;         float al[3], sa = 0.f;
; #pragma unroll
;         for (int p = 0; p < 3; ++p) { al[p] = __expf(ls[p] - mx); sa += al[p]; }
;         const float isa = 1.f / sa; float o[16];
; #pragma unroll
;         for (int i = 0; i < 16; ++i) o[i] = 0.f;
; #pragma unroll
;         for (int p = 0; p < 3; ++p) { const float a = al[p] * isa; const u32x4* src = (const u32x4*)(WSP(bf16_t, WS_OSWA) + ((size_t)p * S_ + t) * 1024 + 16 * lane);
; #pragma unroll
;             for (int q = 0; q < 2; ++q) { const u32x4 w = src[q];
; #pragma unroll
;                 for (int i = 0; i < 4; ++i) { o[q * 8 + 2 * i] += a * bf_lo(w[i]); o[q * 8 + 2 * i + 1] += a * bf_hi(w[i]); } } }
.LBB0_1254:
	v_lshl_add_u64 v[30:31], s[10:11], 0, v[24:25]
	v_add_co_u32_e64 v60, s[4:5], s9, v30
	v_lshl_add_u64 v[28:29], s[10:11], 0, v[26:27]
	s_nop 0
	v_addc_co_u32_e64 v61, s[4:5], 0, v31, s[4:5]
	v_add_co_u32_e64 v66, s[4:5], s36, v30
	v_add_co_u32_e32 v64, vcc, 0x1200000, v28
	s_nop 0
	v_addc_co_u32_e64 v67, s[4:5], 0, v31, s[4:5]
	v_add_co_u32_e64 v72, s[4:5], s37, v30
	v_lshl_add_u64 v[62:63], v[30:31], 0, s[22:23]
	v_lshl_add_u64 v[70:71], v[30:31], 0, s[24:25]
	v_addc_co_u32_e64 v73, s[4:5], 0, v31, s[4:5]
	v_addc_co_u32_e32 v65, vcc, 0, v29, vcc
	global_load_dwordx4 v[6:9], v[18:19], off offset:16
	global_load_dwordx4 v[10:13], v[18:19], off
	global_load_dwordx4 v[2:5], v[18:19], off offset:48
	global_load_dwordx4 v[14:17], v[18:19], off offset:32
	global_load_dwordx4 v[44:47], v[60:61], off
	global_load_dwordx4 v[48:51], v[66:67], off
	global_load_dwordx4 v[52:55], v[62:63], off offset:16
	global_load_dwordx4 v[56:59], v[70:71], off offset:16
	v_add_co_u32_e32 v70, vcc, 0x1280000, v28
	global_load_dwordx4 v[60:63], v[72:73], off
	global_load_dword v43, v[64:65], off
	v_addc_co_u32_e32 v71, vcc, 0, v29, vcc
	v_add_co_u32_e32 v28, vcc, 0x1300000, v28
	v_lshl_add_u64 v[68:69], v[30:31], 0, s[18:19]
	s_nop 0
	v_addc_co_u32_e32 v29, vcc, 0, v29, vcc
	global_load_dword v90, v[70:71], off
	global_load_dword v91, v[28:29], off
	global_load_dwordx4 v[64:67], v[68:69], off offset:16
	v_lshl_add_u64 v[32:33], s[10:11], 0, v[22:23]
	v_add_co_u32_e64 v32, s[4:5], s42, v32
	v_lshl_add_u64 v[34:35], v[30:31], 0, s[38:39]
	s_nop 0
	v_addc_co_u32_e64 v33, s[4:5], 0, v33, s[4:5]
	v_add_co_u32_e64 v30, s[4:5], s43, v30
	s_add_i32 s8, s8, s26
	s_nop 0
	v_addc_co_u32_e64 v31, s[4:5], 0, v31, s[4:5]
	v_lshl_add_u64 v[22:23], v[22:23], 0, s[12:13]
	v_lshl_add_u64 v[24:25], v[24:25], 0, s[14:15]
	v_lshl_add_u64 v[26:27], v[26:27], 0, s[16:17]
	s_cmpk_lt_i32 s8, 0x4000
	s_waitcnt vmcnt(8)
	v_lshlrev_b32_e32 v69, 16, v47
	s_waitcnt vmcnt(7)
	v_lshlrev_b32_e32 v70, 16, v48
	v_mov_b32_e32 v28, v14
	v_mov_b32_e32 v29, v16
	v_mov_b32_e32 v16, v15
	v_mov_b32_e32 v14, v10
	s_waitcnt vmcnt(3)
	v_max_f32_e32 v86, v43, v43
	v_max_f32_e32 v86, 0xf149f2ca, v86
	v_mov_b32_e32 v15, v12
	v_mov_b32_e32 v12, v11
	v_mov_b32_e32 v10, v6
	v_mov_b32_e32 v11, v8
	v_mov_b32_e32 v8, v7
	s_waitcnt vmcnt(1)
	v_max3_f32 v92, v86, v90, v91
	v_sub_f32_e32 v43, v43, v92
	v_sub_f32_e32 v90, v90, v92
	v_mul_f32_e32 v43, 0x3fb8aa3b, v43
	v_sub_f32_e32 v91, v91, v92
	v_mul_f32_e32 v90, 0x3fb8aa3b, v90
	v_exp_f32_e32 v43, v43
	v_mul_f32_e32 v91, 0x3fb8aa3b, v91
	v_exp_f32_e32 v92, v90
	v_exp_f32_e32 v91, v91
	v_add_f32_e32 v90, 0, v43
	v_mov_b32_e32 v6, v2
	v_add_f32_e32 v90, v92, v90
	v_add_f32_e32 v90, v91, v90
	v_div_scale_f32 v93, s[4:5], v90, v90, 1.0
	v_rcp_f32_e32 v95, v93
	v_div_scale_f32 v94, vcc, 1.0, v90, 1.0
	v_mov_b32_e32 v7, v4
	v_fma_f32 v96, -v93, v95, 1.0
	v_fmac_f32_e32 v95, v96, v95
	v_mul_f32_e32 v96, v94, v95
	v_fma_f32 v97, -v93, v96, v94
	v_fmac_f32_e32 v96, v97, v95
	v_fma_f32 v93, -v93, v96, v94
	v_div_fmas_f32 v93, v93, v95, v96
	v_div_fixup_f32 v93, v93, v90, 1.0
	v_mov_b32_e32 v4, v3
	v_lshlrev_b32_e32 v3, 16, v45
	v_lshlrev_b32_e32 v2, 16, v44
	v_and_b32_e32 v45, 0xffff0000, v45
	v_and_b32_e32 v44, 0xffff0000, v44
	v_mul_f32_e32 v90, v43, v93
	v_and_b32_e32 v48, 0xffff0000, v48
	v_lshlrev_b32_e32 v71, 16, v49
	v_and_b32_e32 v49, 0xffff0000, v49
	s_waitcnt vmcnt(0)
	v_lshlrev_b32_e32 v87, 16, v65
	v_lshlrev_b32_e32 v86, 16, v64
	v_and_b32_e32 v65, 0xffff0000, v65
	v_and_b32_e32 v64, 0xffff0000, v64
	v_lshlrev_b32_e32 v89, 16, v67
	v_lshlrev_b32_e32 v88, 16, v66
	v_mul_f32_e32 v92, v92, v93
	v_pk_fma_f32 v[2:3], v[90:91], v[2:3], 0 op_sel_hi:[0,1,0]
	v_pk_fma_f32 v[44:45], v[90:91], v[44:45], 0 op_sel_hi:[0,1,0]
	v_lshlrev_b32_e32 v74, 16, v52
	v_and_b32_e32 v52, 0xffff0000, v52
	v_lshlrev_b32_e32 v75, 16, v53
	v_and_b32_e32 v53, 0xffff0000, v53
	v_lshlrev_b32_e32 v76, 16, v54
	v_lshlrev_b32_e32 v77, 16, v55
	v_lshlrev_b32_e32 v83, 16, v61
	v_lshlrev_b32_e32 v82, 16, v60
	v_and_b32_e32 v61, 0xffff0000, v61
	v_and_b32_e32 v60, 0xffff0000, v60
	v_and_b32_e32 v67, 0xffff0000, v67
	v_and_b32_e32 v66, 0xffff0000, v66
	v_mul_f32_e32 v94, v91, v93
	v_pk_fma_f32 v[64:65], v[90:91], v[64:65], 0 op_sel_hi:[0,1,0]
	v_pk_fma_f32 v[88:89], v[90:91], v[88:89], 0 op_sel_hi:[0,1,0]
	v_pk_fma_f32 v[2:3], v[92:93], v[70:71], v[2:3] op_sel_hi:[0,1,1]
	v_pk_fma_f32 v[44:45], v[92:93], v[48:49], v[44:45] op_sel_hi:[0,1,1]
	v_lshlrev_b32_e32 v68, 16, v46
	v_and_b32_e32 v54, 0xffff0000, v54
	v_and_b32_e32 v55, 0xffff0000, v55
	v_lshlrev_b32_e32 v79, 16, v57
	v_lshlrev_b32_e32 v78, 16, v56
	v_and_b32_e32 v57, 0xffff0000, v57
	v_and_b32_e32 v56, 0xffff0000, v56
	v_lshlrev_b32_e32 v81, 16, v59
	v_lshlrev_b32_e32 v80, 16, v58
	v_pk_fma_f32 v[66:67], v[90:91], v[66:67], 0 op_sel_hi:[0,1,0]
	v_pk_fma_f32 v[52:53], v[92:93], v[52:53], v[64:65] op_sel_hi:[0,1,1]
	v_pk_fma_f32 v[64:65], v[92:93], v[76:77], v[88:89] op_sel_hi:[0,1,1]
	v_pk_fma_f32 v[2:3], v[94:95], v[82:83], v[2:3] op_sel_hi:[0,1,1]
	v_pk_fma_f32 v[44:45], v[94:95], v[60:61], v[44:45] op_sel_hi:[0,1,1]
	v_and_b32_e32 v47, 0xffff0000, v47
	v_and_b32_e32 v46, 0xffff0000, v46
	v_lshlrev_b32_e32 v72, 16, v50
	v_lshlrev_b32_e32 v73, 16, v51
	v_pk_fma_f32 v[68:69], v[90:91], v[68:69], 0 op_sel_hi:[0,1,0]
	v_pk_fma_f32 v[54:55], v[92:93], v[54:55], v[66:67] op_sel_hi:[0,1,1]
	v_pk_fma_f32 v[52:53], v[94:95], v[56:57], v[52:53] op_sel_hi:[0,1,1]
	v_pk_fma_f32 v[56:57], v[94:95], v[80:81], v[64:65] op_sel_hi:[0,1,1]
	v_pk_mul_f32 v[64:65], v[2:3], v[2:3]
	v_pk_mul_f32 v[66:67], v[44:45], v[44:45]
	v_and_b32_e32 v50, 0xffff0000, v50
; __device__ __forceinline__ unsigned pk2(float lo, float hi) { return f2bf(lo) | (f2bf(hi) << 16); }
; __device__ __forceinline__ void p6_mix(Frame& F) {
;     ...
;         float ss = 0.f;
; #pragma unroll
;         for (int i = 0; i < 16; ++i) ss += o[i] * o[i];
;         float rstd = 1.f / sqrtf(wave_sum(ss) * (1.f / 1024.f) + EPS_);
;         bf16_t* mrow = WSP(bf16_t, WS_MIX) + (size_t)t * DM;
;         { u32x4 w0, w1; const float* gg = INF(I_GOSWA) + 16 * lane;
;           w0.x = pk2(o[0] * rstd * gg[0], o[1] * rstd * gg[1]); w0.y = pk2(o[2] * rstd * gg[2], o[3] * rstd * gg[3]); w0.z = pk2(o[4] * rstd * gg[4], o[5] * rstd * gg[5]); w0.w = pk2(o[6] * rstd * gg[6], o[7] * rstd * gg[7]);
;           w1.x = pk2(o[8] * rstd * gg[8], o[9] * rstd * gg[9]); w1.y = pk2(o[10] * rstd * gg[10], o[11] * rstd * gg[11]); w1.z = pk2(o[12] * rstd * gg[12], o[13] * rstd * gg[13]); w1.w = pk2(o[14] * rstd * gg[14], o[15] * rstd * gg[15]);
;           *(u32x4*)(mrow + 16 * lane) = w0; *(u32x4*)(mrow + 16 * lane + 8) = w1; }
;         { const u32x4* src = (const u32x4*)(WSP(bf16_t, WS_OMLA) + (size_t)t * 1024 + 16 * lane);
; #pragma unroll
;           for (int q = 0; q < 2; ++q) { const u32x4 w = src[q];
; #pragma unroll
;               for (int i = 0; i < 4; ++i) { o[q * 8 + 2 * i] = bf_lo(w[i]); o[q * 8 + 2 * i + 1] = bf_hi(w[i]); } } }
	v_and_b32_e32 v51, 0xffff0000, v51
	v_lshlrev_b32_e32 v85, 16, v63
	v_lshlrev_b32_e32 v84, 16, v62
	v_pk_fma_f32 v[46:47], v[90:91], v[46:47], 0 op_sel_hi:[0,1,0]
	v_pk_fma_f32 v[48:49], v[92:93], v[72:73], v[68:69] op_sel_hi:[0,1,1]
	v_add_f32_e32 v43, v64, v66
	v_and_b32_e32 v63, 0xffff0000, v63
	v_and_b32_e32 v62, 0xffff0000, v62
	v_pk_fma_f32 v[46:47], v[92:93], v[50:51], v[46:47] op_sel_hi:[0,1,1]
	v_pk_fma_f32 v[48:49], v[94:95], v[84:85], v[48:49] op_sel_hi:[0,1,1]
	v_add_f32_e32 v43, v65, v43
	v_pk_fma_f32 v[46:47], v[94:95], v[62:63], v[46:47] op_sel_hi:[0,1,1]
	v_pk_mul_f32 v[68:69], v[48:49], v[48:49]
	v_add_f32_e32 v43, v67, v43
	v_pk_fma_f32 v[86:87], v[90:91], v[86:87], 0 op_sel_hi:[0,1,0]
	v_pk_mul_f32 v[70:71], v[46:47], v[46:47]
	v_add_f32_e32 v43, v68, v43
	v_pk_fma_f32 v[74:75], v[92:93], v[74:75], v[86:87] op_sel_hi:[0,1,1]
	v_add_f32_e32 v43, v70, v43
	v_and_b32_e32 v59, 0xffff0000, v59
	v_and_b32_e32 v58, 0xffff0000, v58
	v_pk_fma_f32 v[50:51], v[94:95], v[78:79], v[74:75] op_sel_hi:[0,1,1]
	v_add_f32_e32 v43, v69, v43
	v_pk_fma_f32 v[54:55], v[94:95], v[58:59], v[54:55] op_sel_hi:[0,1,1]
	v_pk_mul_f32 v[58:59], v[50:51], v[50:51]
	v_add_f32_e32 v43, v71, v43
	v_pk_mul_f32 v[60:61], v[52:53], v[52:53]
	v_add_f32_e32 v43, v58, v43
	v_add_f32_e32 v43, v60, v43
	v_add_f32_e32 v43, v59, v43
	v_add_f32_e32 v43, v61, v43
	v_mov_b32_e32 v62, v55
	v_mov_b32_e32 v63, v57
	v_fmac_f32_e32 v43, v56, v56
	v_pk_mul_f32 v[62:63], v[62:63], v[62:63]
	v_fmac_f32_e32 v43, v54, v54
	v_add_f32_e32 v43, v63, v43
	v_add_f32_e32 v43, v62, v43
	s_waitcnt lgkmcnt(0)
	s_nop 1
	v_add_f32_dpp v43, v43, v43 quad_perm:[1,0,3,2] row_mask:0xf bank_mask:0xf bound_ctrl:1
	s_waitcnt lgkmcnt(0)
	s_nop 1
	v_add_f32_dpp v43, v43, v43 quad_perm:[2,3,0,1] row_mask:0xf bank_mask:0xf bound_ctrl:1
	s_waitcnt lgkmcnt(0)
	s_nop 1
	v_add_f32_dpp v43, v43, v43 row_half_mirror row_mask:0xf bank_mask:0xf bound_ctrl:1
	s_waitcnt lgkmcnt(0)
	s_nop 1
	v_add_f32_dpp v43, v43, v43 row_mirror row_mask:0xf bank_mask:0xf bound_ctrl:1
	ds_bpermute_b32 v58, v39, v43
	s_waitcnt lgkmcnt(0)
	v_add_f32_e32 v43, v43, v58
	ds_bpermute_b32 v58, v40, v43
	s_waitcnt lgkmcnt(0)
	v_add_f32_e32 v43, v43, v58
	v_fmamk_f32 v43, v43, 0x3a800000, v41
	v_mul_f32_e32 v58, 0x4f800000, v43
	v_cmp_gt_f32_e32 vcc, s40, v43
	s_nop 1
	v_cndmask_b32_e32 v43, v43, v58, vcc
	v_sqrt_f32_e32 v58, v43
	s_nop 0
	v_add_u32_e32 v59, -1, v58
	v_add_u32_e32 v60, 1, v58
	v_fma_f32 v61, -v59, v58, v43
	v_fma_f32 v62, -v60, v58, v43
	v_cmp_ge_f32_e64 s[4:5], 0, v61
	s_nop 1
	v_cndmask_b32_e64 v58, v58, v59, s[4:5]
	v_cmp_lt_f32_e64 s[4:5], 0, v62
	s_nop 1
	v_cndmask_b32_e64 v58, v58, v60, s[4:5]
	v_mul_f32_e32 v59, 0x37800000, v58
	v_cndmask_b32_e32 v58, v58, v59, vcc
	v_cmp_class_f32_e32 vcc, v43, v42
	s_nop 1
	v_cndmask_b32_e32 v43, v58, v43, vcc
	v_div_scale_f32 v58, s[4:5], v43, v43, 1.0
	v_rcp_f32_e32 v60, v58
	v_div_scale_f32 v59, vcc, 1.0, v43, 1.0
	v_fma_f32 v61, -v58, v60, 1.0
	v_fmac_f32_e32 v60, v61, v60
	v_mul_f32_e32 v61, v59, v60
	v_fma_f32 v62, -v58, v61, v59
	v_fmac_f32_e32 v61, v62, v60
	v_fma_f32 v58, -v58, v61, v59
	v_div_fmas_f32 v58, v58, v60, v61
	v_div_fixup_f32 v58, v58, v43, 1.0
	v_pk_mul_f32 v[2:3], v[2:3], v[58:59] op_sel_hi:[1,0]
	v_pk_mul_f32 v[48:49], v[48:49], v[58:59] op_sel_hi:[1,0]
	v_pk_mul_f32 v[44:45], v[44:45], v[58:59] op_sel_hi:[1,0]
	v_pk_mul_f32 v[46:47], v[46:47], v[58:59] op_sel_hi:[1,0]
	v_pk_mul_f32 v[50:51], v[50:51], v[58:59] op_sel_hi:[1,0]
	v_pk_mul_f32 v[56:57], v[56:57], v[58:59] op_sel_hi:[1,0]
	v_pk_mul_f32 v[54:55], v[54:55], v[58:59] op_sel_hi:[1,0]
	v_pk_mul_f32 v[2:3], v[14:15], v[2:3]
	v_pk_mul_f32 v[10:11], v[10:11], v[48:49]
	v_pk_mul_f32 v[52:53], v[52:53], v[58:59] op_sel_hi:[1,0]
	v_pk_mul_f32 v[12:13], v[12:13], v[44:45]
	v_pk_mul_f32 v[8:9], v[8:9], v[46:47]
	v_pk_mul_f32 v[14:15], v[28:29], v[50:51]
	v_pk_mul_f32 v[6:7], v[6:7], v[56:57]
	v_pk_mul_f32 v[4:5], v[4:5], v[54:55]
	v_bfe_u32 v45, v2, 16, 1
	v_bfe_u32 v46, v3, 16, 1
	v_bfe_u32 v47, v10, 16, 1
	v_bfe_u32 v48, v11, 16, 1
	v_pk_mul_f32 v[16:17], v[16:17], v[52:53]
	v_bfe_u32 v28, v9, 16, 1
	v_bfe_u32 v29, v8, 16, 1
	v_bfe_u32 v43, v13, 16, 1
	v_bfe_u32 v44, v12, 16, 1
	v_bfe_u32 v49, v5, 16, 1
	v_bfe_u32 v50, v4, 16, 1
	v_bfe_u32 v53, v14, 16, 1
	v_bfe_u32 v54, v15, 16, 1
	v_bfe_u32 v55, v6, 16, 1
	v_bfe_u32 v56, v7, 16, 1
	v_add3_u32 v11, v11, v48, s41
	v_add3_u32 v10, v10, v47, s41
	v_add3_u32 v3, v3, v46, s41
	v_add3_u32 v2, v2, v45, s41
	v_bfe_u32 v51, v17, 16, 1
	v_bfe_u32 v52, v16, 16, 1
	v_add3_u32 v12, v12, v44, s41
	v_add3_u32 v13, v13, v43, s41
	v_add3_u32 v8, v8, v29, s41
	v_add3_u32 v9, v9, v28, s41
	v_add3_u32 v28, v4, v50, s41
	v_add3_u32 v29, v5, v49, s41
	v_add3_u32 v4, v7, v56, s41
	v_add3_u32 v5, v6, v55, s41
	v_add3_u32 v6, v15, v54, s41
	v_add3_u32 v7, v14, v53, s41
	v_lshrrev_b32_e32 v2, 16, v2
	v_lshrrev_b32_e32 v3, 16, v3
	v_lshrrev_b32_e32 v10, 16, v10
	v_lshrrev_b32_e32 v11, 16, v11
	v_add3_u32 v16, v16, v52, s41
	v_add3_u32 v17, v17, v51, s41
	v_lshrrev_b32_e32 v14, 16, v7
	v_lshrrev_b32_e32 v6, 16, v6
	v_lshrrev_b32_e32 v7, 16, v5
	v_lshrrev_b32_e32 v15, 16, v4
	v_and_or_b32 v5, v9, s27, v11
	v_and_or_b32 v4, v8, s27, v10
	v_and_or_b32 v3, v13, s27, v3
	v_and_or_b32 v2, v12, s27, v2
	v_and_or_b32 v9, v29, s27, v15
	v_and_or_b32 v8, v28, s27, v7
	v_and_or_b32 v7, v17, s27, v6
	v_and_or_b32 v6, v16, s27, v14
	global_store_dwordx4 v[32:33], v[2:5], off
	global_store_dwordx4 v[32:33], v[6:9], off offset:16
	global_load_dwordx4 v[2:5], v[34:35], off offset:16
	s_nop 0
	global_load_dwordx4 v[6:9], v[20:21], off offset:32
	global_load_dwordx4 v[10:13], v[30:31], off
	global_load_dwordx4 v[14:17], v[20:21], off
	global_load_dwordx4 v[44:47], v[20:21], off offset:16
	global_load_dwordx4 v[48:51], v[20:21], off offset:48
	s_waitcnt vmcnt(5)
; __device__ __forceinline__ unsigned pk2(float lo, float hi) { return f2bf(lo) | (f2bf(hi) << 16); }
; __device__ __forceinline__ void p6_mix(Frame& F) {
;     ...
;         ss = 0.f;
; #pragma unroll
;         for (int i = 0; i < 16; ++i) ss += o[i] * o[i];
;         rstd = 1.f / sqrtf(wave_sum(ss) * (1.f / 1024.f) + EPS_);
;         { u32x4 w0, w1; const float* gg = INF(I_GOMLA) + 16 * lane;
;           w0.x = pk2(o[0] * rstd * gg[0], o[1] * rstd * gg[1]); w0.y = pk2(o[2] * rstd * gg[2], o[3] * rstd * gg[3]); w0.z = pk2(o[4] * rstd * gg[4], o[5] * rstd * gg[5]); w0.w = pk2(o[6] * rstd * gg[6], o[7] * rstd * gg[7]);
;           w1.x = pk2(o[8] * rstd * gg[8], o[9] * rstd * gg[9]); w1.y = pk2(o[10] * rstd * gg[10], o[11] * rstd * gg[11]); w1.z = pk2(o[12] * rstd * gg[12], o[13] * rstd * gg[13]); w1.w = pk2(o[14] * rstd * gg[14], o[15] * rstd * gg[15]);
;           *(u32x4*)(mrow + 1024 + 16 * lane) = w0; *(u32x4*)(mrow + 1024 + 16 * lane + 8) = w1; }
	v_lshlrev_b32_e32 v29, 16, v3
	v_lshlrev_b32_e32 v28, 16, v2
	s_waitcnt vmcnt(3)
	v_lshlrev_b32_e32 v35, 16, v11
	v_lshlrev_b32_e32 v34, 16, v10
	v_and_b32_e32 v11, 0xffff0000, v11
	v_and_b32_e32 v10, 0xffff0000, v10
	v_pk_mul_f32 v[60:61], v[34:35], v[34:35]
	v_pk_mul_f32 v[62:63], v[10:11], v[10:11]
	s_waitcnt vmcnt(2)
	v_mov_b32_e32 v52, v14
	v_add_f32_e32 v43, v60, v62
	v_mov_b32_e32 v53, v16
	v_mov_b32_e32 v16, v15
	v_lshlrev_b32_e32 v15, 16, v13
	v_lshlrev_b32_e32 v14, 16, v12
	v_add_f32_e32 v43, v61, v43
	v_and_b32_e32 v13, 0xffff0000, v13
	v_and_b32_e32 v12, 0xffff0000, v12
	v_pk_mul_f32 v[64:65], v[14:15], v[14:15]
	v_add_f32_e32 v43, v63, v43
	v_pk_mul_f32 v[66:67], v[12:13], v[12:13]
	v_add_f32_e32 v43, v64, v43
	v_add_f32_e32 v43, v66, v43
	v_add_f32_e32 v43, v65, v43
	v_and_b32_e32 v3, 0xffff0000, v3
	v_and_b32_e32 v2, 0xffff0000, v2
	s_waitcnt vmcnt(1)
	v_mov_b32_e32 v54, v44
	v_mov_b32_e32 v55, v46
	v_mov_b32_e32 v46, v45
	s_waitcnt vmcnt(0)
	v_mov_b32_e32 v44, v48
	v_mov_b32_e32 v45, v50
	v_mov_b32_e32 v50, v49
	v_pk_mul_f32 v[48:49], v[28:29], v[28:29]
	v_add_f32_e32 v43, v67, v43
	v_pk_mul_f32 v[56:57], v[2:3], v[2:3]
	v_add_f32_e32 v43, v48, v43
	v_add_f32_e32 v43, v56, v43
	v_add_f32_e32 v43, v49, v43
	v_mov_b32_e32 v30, v6
	v_mov_b32_e32 v31, v8
	v_mov_b32_e32 v8, v7
	v_lshlrev_b32_e32 v7, 16, v5
	v_lshlrev_b32_e32 v6, 16, v4
	v_and_b32_e32 v5, 0xffff0000, v5
	v_add_f32_e32 v43, v57, v43
	v_and_b32_e32 v4, 0xffff0000, v4
	v_mov_b32_e32 v58, v5
	v_mov_b32_e32 v59, v7
	v_fmac_f32_e32 v43, v6, v6
	v_pk_mul_f32 v[58:59], v[58:59], v[58:59]
	v_fmac_f32_e32 v43, v4, v4
	v_add_f32_e32 v43, v59, v43
	v_add_f32_e32 v43, v58, v43
	s_waitcnt lgkmcnt(0)
	s_nop 1
	v_add_f32_dpp v43, v43, v43 quad_perm:[1,0,3,2] row_mask:0xf bank_mask:0xf bound_ctrl:1
	s_waitcnt lgkmcnt(0)
	s_nop 1
	v_add_f32_dpp v43, v43, v43 quad_perm:[2,3,0,1] row_mask:0xf bank_mask:0xf bound_ctrl:1
	s_waitcnt lgkmcnt(0)
	s_nop 1
	v_add_f32_dpp v43, v43, v43 row_half_mirror row_mask:0xf bank_mask:0xf bound_ctrl:1
	s_waitcnt lgkmcnt(0)
	s_nop 1
	v_add_f32_dpp v43, v43, v43 row_mirror row_mask:0xf bank_mask:0xf bound_ctrl:1
	ds_bpermute_b32 v48, v39, v43
	s_waitcnt lgkmcnt(0)
	v_add_f32_e32 v43, v43, v48
	ds_bpermute_b32 v48, v40, v43
	s_waitcnt lgkmcnt(0)
	v_add_f32_e32 v43, v43, v48
	v_fmamk_f32 v43, v43, 0x3a800000, v41
	v_mul_f32_e32 v48, 0x4f800000, v43
	v_cmp_gt_f32_e32 vcc, s40, v43
	s_nop 1
	v_cndmask_b32_e32 v43, v43, v48, vcc
	v_sqrt_f32_e32 v48, v43
	s_nop 0
	v_add_u32_e32 v49, -1, v48
	v_add_u32_e32 v56, 1, v48
	v_fma_f32 v57, -v49, v48, v43
	v_fma_f32 v58, -v56, v48, v43
	v_cmp_ge_f32_e64 s[4:5], 0, v57
	s_nop 1
	v_cndmask_b32_e64 v48, v48, v49, s[4:5]
	v_cmp_lt_f32_e64 s[4:5], 0, v58
	s_nop 1
	v_cndmask_b32_e64 v48, v48, v56, s[4:5]
	v_mul_f32_e32 v49, 0x37800000, v48
	v_cndmask_b32_e32 v48, v48, v49, vcc
	v_cmp_class_f32_e32 vcc, v43, v42
	s_nop 1
	v_cndmask_b32_e32 v43, v48, v43, vcc
	v_div_scale_f32 v48, s[4:5], v43, v43, 1.0
	v_rcp_f32_e32 v56, v48
	v_div_scale_f32 v49, vcc, 1.0, v43, 1.0
	v_fma_f32 v57, -v48, v56, 1.0
	v_fmac_f32_e32 v56, v57, v56
	v_mul_f32_e32 v57, v49, v56
	v_fma_f32 v58, -v48, v57, v49
	v_fmac_f32_e32 v57, v58, v56
	v_fma_f32 v48, -v48, v57, v49
	v_div_fmas_f32 v48, v48, v56, v57
	v_div_fixup_f32 v48, v48, v43, 1.0
	v_pk_mul_f32 v[34:35], v[48:49], v[34:35] op_sel_hi:[0,1]
	v_pk_mul_f32 v[14:15], v[48:49], v[14:15] op_sel_hi:[0,1]
	v_pk_mul_f32 v[12:13], v[48:49], v[12:13] op_sel_hi:[0,1]
	v_pk_mul_f32 v[10:11], v[48:49], v[10:11] op_sel_hi:[0,1]
	v_pk_mul_f32 v[28:29], v[48:49], v[28:29] op_sel_hi:[0,1]
	v_pk_mul_f32 v[2:3], v[48:49], v[2:3] op_sel_hi:[0,1]
	v_pk_mul_f32 v[6:7], v[48:49], v[6:7] op_sel_hi:[0,1]
	v_pk_mul_f32 v[4:5], v[48:49], v[4:5] op_sel_hi:[0,1]
	v_pk_mul_f32 v[34:35], v[52:53], v[34:35]
	v_pk_mul_f32 v[14:15], v[54:55], v[14:15]
	v_pk_mul_f32 v[12:13], v[46:47], v[12:13]
	v_pk_mul_f32 v[10:11], v[16:17], v[10:11]
	v_pk_mul_f32 v[16:17], v[30:31], v[28:29]
	v_pk_mul_f32 v[2:3], v[8:9], v[2:3]
	v_pk_mul_f32 v[6:7], v[44:45], v[6:7]
	v_pk_mul_f32 v[4:5], v[50:51], v[4:5]
	v_bfe_u32 v8, v13, 16, 1
	v_bfe_u32 v9, v12, 16, 1
	v_bfe_u32 v30, v34, 16, 1
	v_bfe_u32 v31, v35, 16, 1
	v_bfe_u32 v43, v14, 16, 1
	v_bfe_u32 v44, v15, 16, 1
	v_bfe_u32 v28, v11, 16, 1
	v_bfe_u32 v29, v10, 16, 1
	v_bfe_u32 v45, v5, 16, 1
	v_bfe_u32 v46, v4, 16, 1
	v_bfe_u32 v47, v3, 16, 1
	v_bfe_u32 v48, v2, 16, 1
	v_bfe_u32 v49, v16, 16, 1
	v_bfe_u32 v50, v17, 16, 1
	v_bfe_u32 v51, v6, 16, 1
	v_bfe_u32 v52, v7, 16, 1
	v_add3_u32 v9, v12, v9, s41
	v_add3_u32 v8, v13, v8, s41
	v_add3_u32 v12, v15, v44, s41
	v_add3_u32 v13, v14, v43, s41
	v_add3_u32 v14, v35, v31, s41
	v_add3_u32 v15, v34, v30, s41
	v_add3_u32 v10, v10, v29, s41
	v_add3_u32 v11, v11, v28, s41
	v_add3_u32 v28, v2, v48, s41
	v_add3_u32 v29, v3, v47, s41
	v_add3_u32 v30, v4, v46, s41
	v_add3_u32 v31, v5, v45, s41
	v_add3_u32 v2, v7, v52, s41
	v_add3_u32 v3, v6, v51, s41
	v_add3_u32 v4, v17, v50, s41
	v_add3_u32 v5, v16, v49, s41
	v_lshrrev_b32_e32 v6, 16, v15
	v_lshrrev_b32_e32 v7, 16, v14
	v_lshrrev_b32_e32 v13, 16, v13
	v_lshrrev_b32_e32 v12, 16, v12
	v_lshrrev_b32_e32 v14, 16, v5
	v_lshrrev_b32_e32 v15, 16, v4
	v_lshrrev_b32_e32 v16, 16, v3
	v_lshrrev_b32_e32 v17, 16, v2
	v_and_or_b32 v5, v8, s27, v12
	v_and_or_b32 v4, v9, s27, v13
	v_and_or_b32 v3, v11, s27, v7
	v_and_or_b32 v2, v10, s27, v6
	v_and_or_b32 v9, v31, s27, v17
	v_and_or_b32 v8, v30, s27, v16
	v_and_or_b32 v7, v29, s27, v15
	v_and_or_b32 v6, v28, s27, v14
	global_store_dwordx4 v[32:33], v[2:5], off offset:2048
	global_store_dwordx4 v[32:33], v[6:9], off offset:2064
	s_cbranch_scc1 .LBB0_1254

; __device__ __forceinline__ void p14_final(Frame& F) {
;     ...
;         const int* so = WSP(int, WS_SDST) + (size_t)t * 8;
; #pragma unroll 4
;         for (int k = 0; k < 8; ++k) { const unsigned char* yr = ys + (size_t)__builtin_amdgcn_readfirstlane(so[k]) * DM;
; #pragma unroll
;             for (int j = 0; j < 2; ++j) acc_fp8x16(acc + 16 * j, ldu16(yr + 1024 * j, lb1)); }
.LBB0_1766:
	s_add_u32 s8, s14, s0
	s_addc_u32 s9, s15, s1
	global_load_dwordx4 v[0:3], v4, s[8:9]
	s_waitcnt vmcnt(0)
	v_readfirstlane_b32 s8, v0
	v_readfirstlane_b32 s10, v1
	v_readfirstlane_b32 s16, v2
	v_readfirstlane_b32 s18, v3
	s_ashr_i32 s9, s8, 31
	s_ashr_i32 s11, s10, 31
	s_ashr_i32 s17, s16, 31
	s_ashr_i32 s19, s18, 31
	s_lshl_b64 s[8:9], s[8:9], 11
	s_lshl_b64 s[10:11], s[10:11], 11
	s_lshl_b64 s[16:17], s[16:17], 11
	s_lshl_b64 s[18:19], s[18:19], 11
	v_lshl_add_u64 v[94:95], v[6:7], 0, s[8:9]
	v_lshl_add_u64 v[96:97], v[6:7], 0, s[10:11]
	v_lshl_add_u64 v[98:99], v[6:7], 0, s[16:17]
	v_lshl_add_u64 v[100:101], v[6:7], 0, s[18:19]
	global_load_dwordx4 v[0:3], v[94:95], off
	global_load_dwordx4 v[66:69], v[94:95], off offset:1024
	global_load_dwordx4 v[70:73], v[96:97], off
	global_load_dwordx4 v[74:77], v[96:97], off offset:1024
	global_load_dwordx4 v[78:81], v[98:99], off
	global_load_dwordx4 v[82:85], v[98:99], off offset:1024
	global_load_dwordx4 v[86:89], v[100:101], off
	global_load_dwordx4 v[90:93], v[100:101], off offset:1024
	s_add_u32 s0, s0, 16
	s_addc_u32 s1, s1, 0
	s_cmp_eq_u32 s0, 32
	s_waitcnt vmcnt(7)
	v_cvt_pk_f32_fp8_e32 v[94:95], v0
	v_cvt_pk_f32_fp8_sdwa v[96:97], v0 src0_sel:WORD_1
	v_cvt_pk_f32_fp8_e32 v[98:99], v1
	v_cvt_pk_f32_fp8_sdwa v[0:1], v1 src0_sel:WORD_1
	v_cvt_pk_f32_fp8_e32 v[100:101], v2
	v_cvt_pk_f32_fp8_sdwa v[102:103], v2 src0_sel:WORD_1
	v_cvt_pk_f32_fp8_e32 v[104:105], v3
	v_cvt_pk_f32_fp8_sdwa v[2:3], v3 src0_sel:WORD_1
	s_waitcnt vmcnt(6)
	v_cvt_pk_f32_fp8_e32 v[106:107], v66
	v_cvt_pk_f32_fp8_sdwa v[108:109], v66 src0_sel:WORD_1
	v_cvt_pk_f32_fp8_e32 v[110:111], v67
	v_cvt_pk_f32_fp8_sdwa v[66:67], v67 src0_sel:WORD_1
	v_cvt_pk_f32_fp8_e32 v[112:113], v68
	v_cvt_pk_f32_fp8_sdwa v[114:115], v68 src0_sel:WORD_1
	v_cvt_pk_f32_fp8_e32 v[116:117], v69
	v_cvt_pk_f32_fp8_sdwa v[68:69], v69 src0_sel:WORD_1
	s_waitcnt vmcnt(5)
	v_cvt_pk_f32_fp8_e32 v[118:119], v70
	v_cvt_pk_f32_fp8_sdwa v[120:121], v70 src0_sel:WORD_1
	v_cvt_pk_f32_fp8_e32 v[122:123], v71
	v_cvt_pk_f32_fp8_sdwa v[70:71], v71 src0_sel:WORD_1
	v_cvt_pk_f32_fp8_e32 v[124:125], v72
	v_cvt_pk_f32_fp8_sdwa v[126:127], v72 src0_sel:WORD_1
	v_cvt_pk_f32_fp8_e32 v[128:129], v73
	v_cvt_pk_f32_fp8_sdwa v[72:73], v73 src0_sel:WORD_1
	s_waitcnt vmcnt(4)
	v_cvt_pk_f32_fp8_e32 v[130:131], v74
	v_cvt_pk_f32_fp8_sdwa v[132:133], v74 src0_sel:WORD_1
	v_cvt_pk_f32_fp8_e32 v[134:135], v75
	v_cvt_pk_f32_fp8_sdwa v[74:75], v75 src0_sel:WORD_1
	v_cvt_pk_f32_fp8_e32 v[136:137], v76
	v_cvt_pk_f32_fp8_sdwa v[138:139], v76 src0_sel:WORD_1
	v_cvt_pk_f32_fp8_e32 v[140:141], v77
	v_cvt_pk_f32_fp8_sdwa v[76:77], v77 src0_sel:WORD_1
	s_waitcnt vmcnt(3)
	v_cvt_pk_f32_fp8_e32 v[142:143], v78
	v_cvt_pk_f32_fp8_sdwa v[144:145], v78 src0_sel:WORD_1
	v_cvt_pk_f32_fp8_e32 v[146:147], v79
	v_cvt_pk_f32_fp8_sdwa v[78:79], v79 src0_sel:WORD_1
	v_cvt_pk_f32_fp8_e32 v[148:149], v80
	v_cvt_pk_f32_fp8_sdwa v[150:151], v80 src0_sel:WORD_1
	v_cvt_pk_f32_fp8_e32 v[152:153], v81
	v_cvt_pk_f32_fp8_sdwa v[80:81], v81 src0_sel:WORD_1
	s_waitcnt vmcnt(2)
	v_cvt_pk_f32_fp8_e32 v[154:155], v82
	v_cvt_pk_f32_fp8_sdwa v[156:157], v82 src0_sel:WORD_1
	v_cvt_pk_f32_fp8_e32 v[158:159], v83
	v_cvt_pk_f32_fp8_sdwa v[82:83], v83 src0_sel:WORD_1
	v_cvt_pk_f32_fp8_e32 v[160:161], v84
	v_cvt_pk_f32_fp8_sdwa v[162:163], v84 src0_sel:WORD_1
	v_cvt_pk_f32_fp8_e32 v[164:165], v85
	v_cvt_pk_f32_fp8_sdwa v[84:85], v85 src0_sel:WORD_1
	s_waitcnt vmcnt(1)
	v_cvt_pk_f32_fp8_e32 v[166:167], v86
	v_cvt_pk_f32_fp8_sdwa v[168:169], v86 src0_sel:WORD_1
	v_cvt_pk_f32_fp8_e32 v[170:171], v87
	v_cvt_pk_f32_fp8_sdwa v[86:87], v87 src0_sel:WORD_1
	v_cvt_pk_f32_fp8_e32 v[172:173], v88
	v_cvt_pk_f32_fp8_sdwa v[174:175], v88 src0_sel:WORD_1
	v_cvt_pk_f32_fp8_e32 v[176:177], v89
	v_cvt_pk_f32_fp8_sdwa v[88:89], v89 src0_sel:WORD_1
	s_waitcnt vmcnt(0)
	v_cvt_pk_f32_fp8_e32 v[178:179], v90
	v_cvt_pk_f32_fp8_sdwa v[180:181], v90 src0_sel:WORD_1
	v_cvt_pk_f32_fp8_e32 v[182:183], v91
	v_cvt_pk_f32_fp8_sdwa v[90:91], v91 src0_sel:WORD_1
	v_cvt_pk_f32_fp8_e32 v[184:185], v92
	v_cvt_pk_f32_fp8_sdwa v[186:187], v92 src0_sel:WORD_1
	v_cvt_pk_f32_fp8_e32 v[188:189], v93
	v_cvt_pk_f32_fp8_sdwa v[92:93], v93 src0_sel:WORD_1
	v_pk_add_f32 v[40:41], v[40:41], v[94:95]
	v_pk_add_f32 v[44:45], v[44:45], v[96:97]
	v_pk_add_f32 v[46:47], v[46:47], v[98:99]
	v_pk_add_f32 v[0:1], v[48:49], v[0:1]
	v_pk_add_f32 v[48:49], v[50:51], v[100:101]
	v_pk_add_f32 v[50:51], v[52:53], v[102:103]
	v_pk_add_f32 v[52:53], v[54:55], v[104:105]
	v_pk_add_f32 v[2:3], v[56:57], v[2:3]
	v_pk_add_f32 v[42:43], v[42:43], v[106:107]
	v_pk_add_f32 v[36:37], v[36:37], v[108:109]
	v_pk_add_f32 v[34:35], v[34:35], v[110:111]
	v_pk_add_f32 v[32:33], v[32:33], v[66:67]
	v_pk_add_f32 v[30:31], v[30:31], v[112:113]
	v_pk_add_f32 v[28:29], v[28:29], v[114:115]
	v_pk_add_f32 v[26:27], v[26:27], v[116:117]
	v_pk_add_f32 v[38:39], v[38:39], v[68:69]
	v_pk_add_f32 v[40:41], v[40:41], v[118:119]
	v_pk_add_f32 v[44:45], v[44:45], v[120:121]
	v_pk_add_f32 v[46:47], v[46:47], v[122:123]
	v_pk_add_f32 v[0:1], v[0:1], v[70:71]
	v_pk_add_f32 v[48:49], v[48:49], v[124:125]
	v_pk_add_f32 v[50:51], v[50:51], v[126:127]
	v_pk_add_f32 v[52:53], v[52:53], v[128:129]
	v_pk_add_f32 v[2:3], v[2:3], v[72:73]
	v_pk_add_f32 v[42:43], v[42:43], v[130:131]
	v_pk_add_f32 v[36:37], v[36:37], v[132:133]
	v_pk_add_f32 v[34:35], v[34:35], v[134:135]
	v_pk_add_f32 v[32:33], v[32:33], v[74:75]
	v_pk_add_f32 v[30:31], v[30:31], v[136:137]
	v_pk_add_f32 v[28:29], v[28:29], v[138:139]
	v_pk_add_f32 v[26:27], v[26:27], v[140:141]
	v_pk_add_f32 v[38:39], v[38:39], v[76:77]
	v_pk_add_f32 v[40:41], v[40:41], v[142:143]
; __device__ __forceinline__ void p14_final(Frame& F) {
;     ...
;         for (int k = 0; k < 8; ++k) { const unsigned char* yr = ys + (size_t)__builtin_amdgcn_readfirstlane(so[k]) * DM;
; #pragma unroll
;             for (int j = 0; j < 2; ++j) acc_fp8x16(acc + 16 * j, ldu16(yr + 1024 * j, lb1)); }
;         { const unsigned char* yr = ys + (size_t)(shbase + t) * DM;
; #pragma unroll
;             for (int j = 0; j < 2; ++j) acc_fp8x16(acc + 16 * j, ldu16(yr + 1024 * j, lb1)); }
;         float* xr = OUTP + (size_t)t * DM; float ss = 0.f;
;         const bf16_t* x1r = WSP(bf16_t, WS_X1) + (size_t)t * DM;
; #pragma unroll
;         for (int j = 0; j < 2; ++j) { const u32x4 xa = ldu16(x1r + 1024 * j, 2u * lb1), xb = ldu16(x1r + 1024 * j + 8, 2u * lb1);
; #pragma unroll
;             for (int q = 0; q < 4; ++q) { const f32x4 g0 = ldf16(gf + 1024 * j + 4 * q, lb4); const u32x4 xw = q < 2 ? xa : xb;
;                 const float a[4] = {bf_lo(xw[(2 * q) & 3]), bf_hi(xw[(2 * q) & 3]), bf_lo(xw[(2 * q + 1) & 3]), bf_hi(xw[(2 * q + 1) & 3])};
; #pragma unroll
;                 for (int i = 0; i < 4; ++i) acc[j * 16 + q * 4 + i] = a[i] + g0[i] * (acc[j * 16 + q * 4 + i] * (1.f / 16.f)); } }
; #pragma unroll
;         for (int i = 0; i < 32; ++i) ss += acc[i] * acc[i];
	v_pk_add_f32 v[44:45], v[44:45], v[144:145]
	v_pk_add_f32 v[46:47], v[46:47], v[146:147]
	v_pk_add_f32 v[0:1], v[0:1], v[78:79]
	v_pk_add_f32 v[54:55], v[48:49], v[148:149]
	v_pk_add_f32 v[56:57], v[50:51], v[150:151]
	v_pk_add_f32 v[66:67], v[52:53], v[152:153]
	v_pk_add_f32 v[2:3], v[2:3], v[80:81]
	v_pk_add_f32 v[42:43], v[42:43], v[154:155]
	v_pk_add_f32 v[36:37], v[36:37], v[156:157]
	v_pk_add_f32 v[34:35], v[34:35], v[158:159]
	v_pk_add_f32 v[32:33], v[32:33], v[82:83]
	v_pk_add_f32 v[30:31], v[30:31], v[160:161]
	v_pk_add_f32 v[28:29], v[28:29], v[162:163]
	v_pk_add_f32 v[26:27], v[26:27], v[164:165]
	v_pk_add_f32 v[38:39], v[38:39], v[84:85]
	v_pk_add_f32 v[40:41], v[40:41], v[166:167]
	v_pk_add_f32 v[44:45], v[44:45], v[168:169]
	v_pk_add_f32 v[46:47], v[46:47], v[170:171]
	v_pk_add_f32 v[48:49], v[0:1], v[86:87]
	v_pk_add_f32 v[50:51], v[54:55], v[172:173]
	v_pk_add_f32 v[52:53], v[56:57], v[174:175]
	v_pk_add_f32 v[54:55], v[66:67], v[176:177]
	v_pk_add_f32 v[56:57], v[2:3], v[88:89]
	v_pk_add_f32 v[42:43], v[42:43], v[178:179]
	v_pk_add_f32 v[36:37], v[36:37], v[180:181]
	v_pk_add_f32 v[34:35], v[34:35], v[182:183]
	v_pk_add_f32 v[32:33], v[32:33], v[90:91]
	v_pk_add_f32 v[30:31], v[30:31], v[184:185]
	v_pk_add_f32 v[28:29], v[28:29], v[186:187]
	v_pk_add_f32 v[26:27], v[26:27], v[188:189]
	v_pk_add_f32 v[38:39], v[38:39], v[92:93]
	s_cbranch_scc0 .LBB0_1766
	s_lshl_b64 s[0:1], s[2:3], 12
	v_lshl_add_u64 v[122:123], v[24:25], 0, s[0:1]
	global_load_dwordx4 v[66:69], v[122:123], off offset:2064
	global_load_dwordx4 v[70:73], v[122:123], off
	global_load_dwordx4 v[74:77], v[122:123], off offset:16
	s_add_i32 s0, s2, s7
	s_ashr_i32 s1, s0, 31
	s_lshl_b64 s[0:1], s[0:1], 11
	v_lshl_add_u64 v[124:125], v[6:7], 0, s[0:1]
	global_load_dwordx4 v[78:81], v[124:125], off
	global_load_dwordx4 v[82:85], v[124:125], off offset:1024
	global_load_dwordx4 v[86:89], v[10:11], off offset:48
	global_load_dwordx4 v[90:93], v[8:9], off
	global_load_dwordx4 v[94:97], v[8:9], off offset:16
	global_load_dwordx4 v[98:101], v[8:9], off offset:32
	global_load_dwordx4 v[102:105], v[8:9], off offset:48
	global_load_dwordx4 v[106:109], v[122:123], off offset:2048
	global_load_dwordx4 v[110:113], v[10:11], off
	global_load_dwordx4 v[114:117], v[10:11], off offset:32
	global_load_dwordx4 v[118:121], v[10:11], off offset:16
	s_waitcnt vmcnt(10)
	v_cvt_pk_f32_fp8_e32 v[132:133], v78
	v_cvt_pk_f32_fp8_sdwa v[134:135], v78 src0_sel:WORD_1
	v_cvt_pk_f32_fp8_e32 v[136:137], v79
	v_cvt_pk_f32_fp8_sdwa v[78:79], v79 src0_sel:WORD_1
	v_cvt_pk_f32_fp8_sdwa v[140:141], v80 src0_sel:WORD_1
	v_cvt_pk_f32_fp8_e32 v[138:139], v80
	v_cvt_pk_f32_fp8_e32 v[142:143], v81
	v_cvt_pk_f32_fp8_sdwa v[80:81], v81 src0_sel:WORD_1
	v_pk_add_f32 v[40:41], v[40:41], v[132:133]
	v_lshlrev_b32_e32 v124, 16, v70
	v_and_b32_e32 v125, 0xffff0000, v70
	v_pk_add_f32 v[44:45], v[44:45], v[134:135]
	v_pk_add_f32 v[48:49], v[48:49], v[78:79]
	v_pk_mul_f32 v[40:41], v[40:41], s[6:7] op_sel_hi:[1,0]
	v_lshlrev_b32_e32 v70, 16, v71
	v_and_b32_e32 v71, 0xffff0000, v71
	v_lshlrev_b32_e32 v126, 16, v72
	v_and_b32_e32 v127, 0xffff0000, v72
	v_lshlrev_b32_e32 v72, 16, v73
	v_and_b32_e32 v73, 0xffff0000, v73
	v_pk_add_f32 v[52:53], v[52:53], v[140:141]
	v_pk_mul_f32 v[44:45], v[44:45], s[6:7] op_sel_hi:[1,0]
	v_pk_mul_f32 v[48:49], v[48:49], s[6:7] op_sel_hi:[1,0]
	s_waitcnt vmcnt(7)
	v_pk_fma_f32 v[40:41], v[40:41], v[90:91], v[124:125]
	v_lshlrev_b32_e32 v128, 16, v74
	v_and_b32_e32 v129, 0xffff0000, v74
	v_lshlrev_b32_e32 v74, 16, v75
	v_and_b32_e32 v75, 0xffff0000, v75
	v_pk_add_f32 v[46:47], v[46:47], v[136:137]
	v_pk_mul_f32 v[52:53], v[52:53], s[6:7] op_sel_hi:[1,0]
	v_pk_fma_f32 v[44:45], v[44:45], v[92:93], v[70:71]
	s_waitcnt vmcnt(6)
	v_pk_fma_f32 v[48:49], v[48:49], v[96:97], v[72:73]
	v_pk_mul_f32 v[72:73], v[40:41], v[40:41]
	v_pk_add_f32 v[56:57], v[56:57], v[80:81]
	v_pk_mul_f32 v[46:47], v[46:47], s[6:7] op_sel_hi:[1,0]
	s_waitcnt vmcnt(5)
	v_pk_fma_f32 v[52:53], v[52:53], v[100:101], v[74:75]
	v_pk_mul_f32 v[74:75], v[44:45], v[44:45]
	v_add_f32_e32 v72, v72, v73
	v_lshlrev_b32_e32 v130, 16, v76
	v_and_b32_e32 v131, 0xffff0000, v76
	v_lshlrev_b32_e32 v76, 16, v77
	v_and_b32_e32 v77, 0xffff0000, v77
	v_pk_mul_f32 v[56:57], v[56:57], s[6:7] op_sel_hi:[1,0]
	v_pk_fma_f32 v[46:47], v[46:47], v[94:95], v[126:127]
	v_add_f32_e32 v72, v74, v72
	v_cvt_pk_f32_fp8_sdwa v[150:151], v85 src0_sel:WORD_1
	s_waitcnt vmcnt(4)
	v_pk_fma_f32 v[56:57], v[56:57], v[104:105], v[76:77]
	v_pk_mul_f32 v[76:77], v[46:47], v[46:47]
	v_add_f32_e32 v72, v75, v72
	v_pk_add_f32 v[50:51], v[50:51], v[138:139]
	v_add_f32_e32 v72, v76, v72
	v_pk_mul_f32 v[50:51], v[50:51], s[6:7] op_sel_hi:[1,0]
	v_pk_mul_f32 v[78:79], v[48:49], v[48:49]
	v_add_f32_e32 v72, v77, v72
	v_pk_fma_f32 v[50:51], v[50:51], v[98:99], v[128:129]
	v_add_f32_e32 v72, v78, v72
	v_pk_add_f32 v[38:39], v[38:39], v[150:151]
	v_pk_mul_f32 v[80:81], v[50:51], v[50:51]
	v_add_f32_e32 v72, v79, v72
	v_and_b32_e32 v123, 0xffff0000, v69
	v_lshlrev_b32_e32 v122, 16, v69
	v_cvt_pk_f32_fp8_e32 v[144:145], v82
	v_pk_add_f32 v[54:55], v[54:55], v[142:143]
	v_pk_mul_f32 v[38:39], v[38:39], s[6:7] op_sel_hi:[1,0]
	v_add_f32_e32 v72, v80, v72
	v_pk_mul_f32 v[54:55], v[54:55], s[6:7] op_sel_hi:[1,0]
	v_pk_fma_f32 v[38:39], v[38:39], v[88:89], v[122:123]
	v_pk_mul_f32 v[88:89], v[52:53], v[52:53]
	v_add_f32_e32 v72, v81, v72
	v_cvt_pk_f32_fp8_sdwa v[146:147], v82 src0_sel:WORD_1
	v_pk_fma_f32 v[54:55], v[54:55], v[102:103], v[130:131]
	v_add_f32_e32 v72, v88, v72
	v_pk_mul_f32 v[90:91], v[54:55], v[54:55]
	v_add_f32_e32 v72, v89, v72
	v_cvt_pk_f32_fp8_e32 v[148:149], v83
	v_pk_add_f32 v[42:43], v[42:43], v[144:145]
	v_add_f32_e32 v72, v90, v72
	v_pk_mul_f32 v[92:93], v[56:57], v[56:57]
	s_waitcnt vmcnt(3)
; __device__ __forceinline__ float wave_sum(float v) {
; #pragma unroll
;     for (int o = 1; o < 64; o <<= 1) v += __shfl_xor(v, o);
;     return v;
; __device__ __forceinline__ void p14_final(Frame& F) {
;     ...
;                 for (int i = 0; i < 4; ++i) acc[j * 16 + q * 4 + i] = a[i] + g0[i] * (acc[j * 16 + q * 4 + i] * (1.f / 16.f)); } }
; #pragma unroll
;         for (int i = 0; i < 32; ++i) ss += acc[i] * acc[i];
;         const float rstd = 1.f / sqrtf(wave_sum(ss) * (1.f / DM) + EPS_);
; #pragma unroll
;         for (int j = 0; j < 2; ++j)
; #pragma unroll
;             for (int q = 0; q < 4; ++q) { const f32x4 g0 = ldf16(INF(I_FNG) + 1024 * j + 4 * q, lb4); f32x4 o0;
; #pragma unroll
;                 for (int i = 0; i < 4; ++i) o0[i] = acc[j * 16 + q * 4 + i] * rstd * g0[i];
;                 *(f32x4*)((char*)(xr + 1024 * j + 4 * q) + lb4) = o0; }
	v_lshlrev_b32_e32 v94, 16, v106
	v_and_b32_e32 v95, 0xffff0000, v106
	v_pk_mul_f32 v[42:43], v[42:43], s[6:7] op_sel_hi:[1,0]
	v_add_f32_e32 v72, v91, v72
	v_cvt_pk_f32_fp8_sdwa v[82:83], v83 src0_sel:WORD_1
	s_waitcnt vmcnt(2)
	v_pk_fma_f32 v[42:43], v[42:43], v[110:111], v[94:95]
	v_pk_add_f32 v[36:37], v[36:37], v[146:147]
	v_add_f32_e32 v72, v92, v72
	v_pk_mul_f32 v[94:95], v[42:43], v[42:43]
	v_lshlrev_b32_e32 v96, 16, v107
	v_and_b32_e32 v97, 0xffff0000, v107
	v_pk_mul_f32 v[36:37], v[36:37], s[6:7] op_sel_hi:[1,0]
	v_add_f32_e32 v72, v93, v72
	v_cvt_pk_f32_fp8_e32 v[152:153], v84
	v_pk_fma_f32 v[36:37], v[36:37], v[112:113], v[96:97]
	v_pk_add_f32 v[34:35], v[34:35], v[148:149]
	v_add_f32_e32 v72, v94, v72
	v_pk_mul_f32 v[96:97], v[36:37], v[36:37]
	v_lshlrev_b32_e32 v98, 16, v108
	v_and_b32_e32 v99, 0xffff0000, v108
	v_pk_mul_f32 v[34:35], v[34:35], s[6:7] op_sel_hi:[1,0]
	v_add_f32_e32 v72, v95, v72
	v_cvt_pk_f32_fp8_sdwa v[154:155], v84 src0_sel:WORD_1
	s_waitcnt vmcnt(0)
	v_pk_fma_f32 v[34:35], v[34:35], v[118:119], v[98:99]
	v_pk_add_f32 v[32:33], v[32:33], v[82:83]
	v_add_f32_e32 v72, v96, v72
	v_pk_mul_f32 v[98:99], v[34:35], v[34:35]
	v_lshlrev_b32_e32 v82, 16, v109
	v_and_b32_e32 v83, 0xffff0000, v109
	v_pk_mul_f32 v[32:33], v[32:33], s[6:7] op_sel_hi:[1,0]
	v_add_f32_e32 v72, v97, v72
	v_cvt_pk_f32_fp8_e32 v[84:85], v85
	v_pk_fma_f32 v[32:33], v[32:33], v[120:121], v[82:83]
	v_pk_add_f32 v[30:31], v[30:31], v[152:153]
	v_add_f32_e32 v72, v98, v72
	v_pk_mul_f32 v[82:83], v[32:33], v[32:33]
	v_lshlrev_b32_e32 v100, 16, v66
	v_and_b32_e32 v101, 0xffff0000, v66
	v_pk_mul_f32 v[30:31], v[30:31], s[6:7] op_sel_hi:[1,0]
	v_add_f32_e32 v72, v99, v72
	v_pk_fma_f32 v[30:31], v[30:31], v[114:115], v[100:101]
	v_pk_add_f32 v[28:29], v[28:29], v[154:155]
	v_add_f32_e32 v72, v82, v72
	v_pk_mul_f32 v[100:101], v[30:31], v[30:31]
	v_lshlrev_b32_e32 v66, 16, v67
	v_and_b32_e32 v67, 0xffff0000, v67
	v_pk_mul_f32 v[28:29], v[28:29], s[6:7] op_sel_hi:[1,0]
	v_add_f32_e32 v72, v83, v72
	v_pk_fma_f32 v[28:29], v[28:29], v[116:117], v[66:67]
	v_pk_add_f32 v[26:27], v[26:27], v[84:85]
	v_add_f32_e32 v72, v100, v72
	v_pk_mul_f32 v[66:67], v[28:29], v[28:29]
	v_lshlrev_b32_e32 v84, 16, v68
	v_and_b32_e32 v85, 0xffff0000, v68
	v_pk_mul_f32 v[26:27], v[26:27], s[6:7] op_sel_hi:[1,0]
	v_add_f32_e32 v72, v101, v72
	v_pk_fma_f32 v[26:27], v[26:27], v[86:87], v[84:85]
	v_add_f32_e32 v66, v66, v72
	v_pk_mul_f32 v[68:69], v[26:27], v[26:27]
	v_add_f32_e32 v66, v67, v66
	v_add_f32_e32 v66, v68, v66
	v_pk_mul_f32 v[70:71], v[38:39], v[38:39]
	v_add_f32_e32 v66, v69, v66
	v_add_f32_e32 v66, v70, v66
	v_add_f32_e32 v66, v71, v66
	s_waitcnt lgkmcnt(0)
	s_nop 1
	v_add_f32_dpp v66, v66, v66 quad_perm:[1,0,3,2] row_mask:0xf bank_mask:0xf bound_ctrl:1
	s_waitcnt lgkmcnt(0)
	s_nop 1
	v_add_f32_dpp v66, v66, v66 quad_perm:[2,3,0,1] row_mask:0xf bank_mask:0xf bound_ctrl:1
	s_waitcnt lgkmcnt(0)
	s_nop 1
	v_add_f32_dpp v66, v66, v66 row_half_mirror row_mask:0xf bank_mask:0xf bound_ctrl:1
	s_waitcnt lgkmcnt(0)
	s_nop 1
	v_add_f32_dpp v66, v66, v66 row_mirror row_mask:0xf bank_mask:0xf bound_ctrl:1
	ds_bpermute_b32 v67, v62, v66
	s_waitcnt lgkmcnt(0)
	v_add_f32_e32 v66, v66, v67
	ds_bpermute_b32 v67, v63, v66
	s_waitcnt lgkmcnt(0)
	v_add_f32_e32 v66, v66, v67
	v_fmamk_f32 v66, v66, 0x3a000000, v64
	v_mul_f32_e32 v67, 0x4f800000, v66
	v_cmp_gt_f32_e32 vcc, s12, v66
	s_nop 1
	v_cndmask_b32_e32 v66, v66, v67, vcc
	v_sqrt_f32_e32 v67, v66
	s_nop 0
	v_add_u32_e32 v68, -1, v67
	v_fma_f32 v69, -v68, v67, v66
	v_cmp_ge_f32_e64 s[0:1], 0, v69
	v_add_u32_e32 v69, 1, v67
	s_nop 0
	v_cndmask_b32_e64 v68, v67, v68, s[0:1]
	v_fma_f32 v67, -v69, v67, v66
	v_cmp_lt_f32_e64 s[0:1], 0, v67
	s_nop 1
	v_cndmask_b32_e64 v67, v68, v69, s[0:1]
	v_mul_f32_e32 v68, 0x37800000, v67
	v_cndmask_b32_e32 v67, v67, v68, vcc
	v_cmp_class_f32_e32 vcc, v66, v65
	s_nop 1
	v_cndmask_b32_e32 v68, v67, v66, vcc
	v_div_scale_f32 v69, s[0:1], v68, v68, 1.0
	v_rcp_f32_e32 v70, v69
	s_lshl_b64 s[0:1], s[2:3], 13
	v_lshl_add_u64 v[66:67], v[12:13], 0, s[0:1]
	s_add_i32 s2, s2, s26
	v_fma_f32 v71, -v69, v70, 1.0
	v_fmac_f32_e32 v70, v71, v70
	v_div_scale_f32 v71, vcc, 1.0, v68, 1.0
	v_mul_f32_e32 v72, v71, v70
	v_fma_f32 v73, -v69, v72, v71
	v_fmac_f32_e32 v72, v73, v70
	v_fma_f32 v69, -v69, v72, v71
	v_div_fmas_f32 v69, v69, v70, v72
	v_div_fixup_f32 v68, v69, v68, 1.0
	v_pk_mul_f32 v[40:41], v[40:41], v[68:69] op_sel_hi:[1,0]
	v_pk_mul_f32 v[44:45], v[44:45], v[68:69] op_sel_hi:[1,0]
	v_pk_mul_f32 v[0:1], v[192:193], v[40:41]
	v_pk_mul_f32 v[2:3], v[194:195], v[44:45]
	global_store_dwordx4 v[66:67], v[0:3], off
	v_pk_mul_f32 v[40:41], v[48:49], v[68:69] op_sel_hi:[1,0]
	v_pk_mul_f32 v[44:45], v[46:47], v[68:69] op_sel_hi:[1,0]
	v_pk_mul_f32 v[36:37], v[36:37], v[68:69] op_sel_hi:[1,0]
	v_pk_mul_f32 v[42:43], v[42:43], v[68:69] op_sel_hi:[1,0]
	v_pk_mul_f32 v[32:33], v[32:33], v[68:69] op_sel_hi:[1,0]
	v_pk_mul_f32 v[34:35], v[34:35], v[68:69] op_sel_hi:[1,0]
	v_pk_mul_f32 v[28:29], v[28:29], v[68:69] op_sel_hi:[1,0]
	v_pk_mul_f32 v[30:31], v[30:31], v[68:69] op_sel_hi:[1,0]
	v_pk_mul_f32 v[26:27], v[26:27], v[68:69] op_sel_hi:[1,0]
	s_cmpk_gt_i32 s2, 0x3fff
	v_pk_mul_f32 v[224:225], v[196:197], v[44:45]
	v_pk_mul_f32 v[226:227], v[198:199], v[40:41]
	global_store_dwordx4 v[66:67], v[224:227], off offset:16
	v_pk_mul_f32 v[40:41], v[52:53], v[68:69] op_sel_hi:[1,0]
	v_pk_mul_f32 v[44:45], v[50:51], v[68:69] op_sel_hi:[1,0]
	v_pk_mul_f32 v[2:3], v[202:203], v[40:41]
	v_pk_mul_f32 v[0:1], v[200:201], v[44:45]
	global_store_dwordx4 v[66:67], v[0:3], off offset:32
	v_pk_mul_f32 v[40:41], v[56:57], v[68:69] op_sel_hi:[1,0]
	v_pk_mul_f32 v[44:45], v[54:55], v[68:69] op_sel_hi:[1,0]
	v_pk_mul_f32 v[226:227], v[206:207], v[40:41]
	v_pk_mul_f32 v[224:225], v[204:205], v[44:45]
	global_store_dwordx4 v[66:67], v[224:227], off offset:48
	v_add_co_u32_e32 v40, vcc, s13, v66
	s_nop 0
	v_pk_mul_f32 v[0:1], v[208:209], v[42:43]
	v_addc_co_u32_e32 v41, vcc, 0, v67, vcc
	v_pk_mul_f32 v[2:3], v[210:211], v[36:37]
	global_store_dwordx4 v[40:41], v[0:3], off
	v_pk_mul_f32 v[224:225], v[212:213], v[34:35]
	v_pk_mul_f32 v[226:227], v[214:215], v[32:33]
	global_store_dwordx4 v[40:41], v[224:227], off offset:16
	v_pk_mul_f32 v[0:1], v[216:217], v[30:31]
	v_pk_mul_f32 v[2:3], v[218:219], v[28:29]
	global_store_dwordx4 v[40:41], v[0:3], off offset:32
	v_pk_mul_f32 v[28:29], v[38:39], v[68:69] op_sel_hi:[1,0]
	v_pk_mul_f32 v[224:225], v[220:221], v[26:27]
	v_pk_mul_f32 v[226:227], v[222:223], v[28:29]
	global_store_dwordx4 v[40:41], v[224:227], off offset:48
	s_cbranch_scc0 .LBB0_1765
